# grid barrier release: last XCD leader publishes gen+1 to all 8 relay words itself (umax), TOPGEN/own relay updates made idempotent umax; on top of early invalidate
# baseline (speedup 1.0000x reference)
; __device__ __forceinline__ unsigned xb_ld(unsigned* p)              { return __hip_atomic_load(p, __ATOMIC_RELAXED, __HIP_MEMORY_SCOPE_AGENT); }
; __device__ __forceinline__ unsigned xb_add(unsigned* p, unsigned v) { return __hip_atomic_fetch_add(p, v, __ATOMIC_RELAXED, __HIP_MEMORY_SCOPE_AGENT); }
; #define XB_SPIN(cond, bar) do { unsigned _sp = 0; while (cond) { __builtin_amdgcn_s_sleep(1); \
;     if ((++_sp & 255u) == 0u) { if (xb_ld(&(bar)[XB_TMO])) break; if (_sp > XB_SPIN_CAP) { atomicAdd(&(bar)[XB_TMO], 1u); break; } } } } while (0)
; __device__ __forceinline__ void xcd_barrier(const XcdBarrier& b) {
;     ...
;             const unsigned og = xb_add(&bar[XB_TOP], 1u);
;             const unsigned tg = og / nx;
;             if (og + 1u == (tg + 1u) * nx) xb_add(&bar[XB_TOPGEN], 1u);
;             else XB_SPIN(xb_ld(&bar[XB_TOPGEN]) == tg, bar);
;             __builtin_amdgcn_fence(__ATOMIC_ACQUIRE, "agent");
;             xb_add(&bar[XB_XGEN(b.x)], 1u);
;             asm volatile("s_waitcnt vmcnt(0)" ::: "memory");
.LBB0_94:
	s_or_b64 exec, exec, s[4:5]
	s_and_saveexec_b64 s[4:5], s[8:9]
	s_cbranch_execz .LBB0_96
	v_add_u32_e32 v1, 1, v4
	global_atomic_umax v[2:3], v1, off
	s_getreg_b32 s10, hwreg(HW_REG_XCC_ID, 0, 4)
	s_lshl_b32 s10, s10, 8
	s_nop 0
	v_mov_b32_e32 v2, s10
	v_sub_u32_e32 v2, 0x2400, v2
	global_atomic_umax v2, v1, s[2:3]
	global_atomic_umax v2, v1, s[2:3] offset:256
	global_atomic_umax v2, v1, s[2:3] offset:512
	global_atomic_umax v2, v1, s[2:3] offset:768
	global_atomic_umax v2, v1, s[2:3] offset:1024
	global_atomic_umax v2, v1, s[2:3] offset:1280
	global_atomic_umax v2, v1, s[2:3] offset:1536
	global_atomic_umax v2, v1, s[2:3] offset:1792
.LBB0_96:
	s_or_b64 exec, exec, s[4:5]
	v_mov_b32_e32 v1, 0x2000
	v_add_u32_e32 v2, 1, v4
	s_waitcnt vmcnt(0)
	global_atomic_umax v1, v2, s[2:3] offset:1024
	s_waitcnt vmcnt(0)

; __device__ __forceinline__ unsigned xb_ld(unsigned* p)              { return __hip_atomic_load(p, __ATOMIC_RELAXED, __HIP_MEMORY_SCOPE_AGENT); }
; __device__ __forceinline__ unsigned xb_add(unsigned* p, unsigned v) { return __hip_atomic_fetch_add(p, v, __ATOMIC_RELAXED, __HIP_MEMORY_SCOPE_AGENT); }
; #define XB_SPIN(cond, bar) do { unsigned _sp = 0; while (cond) { __builtin_amdgcn_s_sleep(1); \
;     if ((++_sp & 255u) == 0u) { if (xb_ld(&(bar)[XB_TMO])) break; if (_sp > XB_SPIN_CAP) { atomicAdd(&(bar)[XB_TMO], 1u); break; } } } } while (0)
; __device__ __forceinline__ void xcd_barrier(const XcdBarrier& b) {
;     ...
;             const unsigned og = xb_add(&bar[XB_TOP], 1u);
;             const unsigned tg = og / nx;
;             if (og + 1u == (tg + 1u) * nx) xb_add(&bar[XB_TOPGEN], 1u);
;             else XB_SPIN(xb_ld(&bar[XB_TOPGEN]) == tg, bar);
;             __builtin_amdgcn_fence(__ATOMIC_ACQUIRE, "agent");
;             xb_add(&bar[XB_XGEN(b.x)], 1u);
;             asm volatile("s_waitcnt vmcnt(0)" ::: "memory");
.LBB0_255:
	s_or_b64 exec, exec, s[4:5]
	s_and_saveexec_b64 s[4:5], s[8:9]
	s_cbranch_execz .LBB0_257
	v_add_u32_e32 v4, 1, v4
	global_atomic_umax v[2:3], v4, off
	s_getreg_b32 s10, hwreg(HW_REG_XCC_ID, 0, 4)
	s_lshl_b32 s10, s10, 8
	s_nop 0
	v_mov_b32_e32 v2, s10
	v_sub_u32_e32 v2, 0x2400, v2
	global_atomic_umax v2, v4, s[2:3]
	global_atomic_umax v2, v4, s[2:3] offset:256
	global_atomic_umax v2, v4, s[2:3] offset:512
	global_atomic_umax v2, v4, s[2:3] offset:768
	global_atomic_umax v2, v4, s[2:3] offset:1024
	global_atomic_umax v2, v4, s[2:3] offset:1280
	global_atomic_umax v2, v4, s[2:3] offset:1536
	global_atomic_umax v2, v4, s[2:3] offset:1792
	s_nop 1
	v_add_u32_e32 v4, -1, v4
.LBB0_257:
	s_or_b64 exec, exec, s[4:5]
	v_mov_b32_e32 v2, 0x2000
	v_add_u32_e32 v3, 1, v4
	s_waitcnt vmcnt(0)
	global_atomic_umax v2, v3, s[2:3] offset:1024
	s_waitcnt vmcnt(0)

; __device__ __forceinline__ unsigned xb_ld(unsigned* p)              { return __hip_atomic_load(p, __ATOMIC_RELAXED, __HIP_MEMORY_SCOPE_AGENT); }
; __device__ __forceinline__ unsigned xb_add(unsigned* p, unsigned v) { return __hip_atomic_fetch_add(p, v, __ATOMIC_RELAXED, __HIP_MEMORY_SCOPE_AGENT); }
; #define XB_SPIN(cond, bar) do { unsigned _sp = 0; while (cond) { __builtin_amdgcn_s_sleep(1); \
;     if ((++_sp & 255u) == 0u) { if (xb_ld(&(bar)[XB_TMO])) break; if (_sp > XB_SPIN_CAP) { atomicAdd(&(bar)[XB_TMO], 1u); break; } } } } while (0)
; __device__ __forceinline__ void xcd_barrier(const XcdBarrier& b) {
;     ...
;             const unsigned og = xb_add(&bar[XB_TOP], 1u);
;             const unsigned tg = og / nx;
;             if (og + 1u == (tg + 1u) * nx) xb_add(&bar[XB_TOPGEN], 1u);
;             else XB_SPIN(xb_ld(&bar[XB_TOPGEN]) == tg, bar);
;             __builtin_amdgcn_fence(__ATOMIC_ACQUIRE, "agent");
;             xb_add(&bar[XB_XGEN(b.x)], 1u);
;             asm volatile("s_waitcnt vmcnt(0)" ::: "memory");
.LBB0_4460:
	s_or_b64 exec, exec, s[4:5]
	s_and_saveexec_b64 s[4:5], s[8:9]
	s_cbranch_execz .LBB0_4462
	v_add_u32_e32 v1, 1, v4
	global_atomic_umax v[2:3], v1, off
	s_getreg_b32 s10, hwreg(HW_REG_XCC_ID, 0, 4)
	s_lshl_b32 s10, s10, 8
	s_nop 0
	v_mov_b32_e32 v2, s10
	v_sub_u32_e32 v2, 0x2400, v2
	global_atomic_umax v2, v1, s[0:1]
	global_atomic_umax v2, v1, s[0:1] offset:256
	global_atomic_umax v2, v1, s[0:1] offset:512
	global_atomic_umax v2, v1, s[0:1] offset:768
	global_atomic_umax v2, v1, s[0:1] offset:1024
	global_atomic_umax v2, v1, s[0:1] offset:1280
	global_atomic_umax v2, v1, s[0:1] offset:1536
	global_atomic_umax v2, v1, s[0:1] offset:1792
.LBB0_4462:
	s_or_b64 exec, exec, s[4:5]
	v_mov_b32_e32 v1, 0x2000
	v_add_u32_e32 v2, 1, v4
	s_waitcnt vmcnt(0)
	global_atomic_umax v1, v2, s[0:1] offset:1024
	s_waitcnt vmcnt(0)
